# pipelined diff-attention + ssd_local A_log load issued with the dt loads + ssd_out h_in fragment loads issued up front
# baseline (speedup 1.0000x reference)
.LBB0_418:
	s_and_b32 s55, s45, 0x1ff
	s_lshl_b32 s56, s55, 6
	v_add_lshl_u32 v0, s56, v85, 5
	global_load_dword v0, v0, s[28:29]
	s_nop 0
	global_load_dword v1, v209, s[30:31]
	global_load_dword v255, v209, s[34:35]
	s_mov_b32 s36, 0xbfb8aa3b
	s_waitcnt vmcnt(0)
	v_add_f32_e32 v0, v0, v1
	v_max_f32_e32 v2, 0, v0
	v_mul_f32_e64 v0, |v0|, s36
	v_exp_f32_e32 v3, v0
	s_mov_b32 s36, 0x3f2aaaab
	v_add_f32_e32 v4, 1.0, v3
	v_add_f32_e32 v0, -1.0, v4
	v_sub_f32_e32 v1, v0, v4
	v_add_f32_e32 v1, 1.0, v1
	v_sub_f32_e32 v0, v3, v0
	v_add_f32_e32 v5, v0, v1
	v_frexp_mant_f32_e32 v0, v4
	v_cmp_gt_f32_e32 vcc, s36, v0
	v_cvt_f64_f32_e32 v[0:1], v4
	v_frexp_exp_i32_f64_e32 v0, v[0:1]
	v_subbrev_co_u32_e32 v0, vcc, 0, v0, vcc
	v_sub_u32_e32 v1, 0, v0
	v_ldexp_f32 v4, v4, v1
	v_ldexp_f32 v1, v5, v1
	v_add_f32_e32 v5, -1.0, v4
	v_add_f32_e32 v6, 1.0, v5
	v_sub_f32_e32 v6, v4, v6
	v_add_f32_e32 v6, v1, v6
	v_add_f32_e32 v7, v5, v6
	v_sub_f32_e32 v5, v7, v5
	v_sub_f32_e32 v5, v6, v5
	v_add_f32_e32 v6, 1.0, v4
	v_add_f32_e32 v8, -1.0, v6
	v_sub_f32_e32 v4, v4, v8
	v_add_f32_e32 v1, v1, v4
	v_add_f32_e32 v4, v6, v1
	v_sub_f32_e32 v6, v4, v6
	v_sub_f32_e32 v1, v1, v6
	v_rcp_f32_e32 v6, v4
	v_cvt_f32_i32_e32 v0, v0
	s_mov_b32 s36, 0x3f317218
	v_mul_f32_e32 v8, v7, v6
	v_mul_f32_e32 v9, v4, v8
	v_fma_f32 v10, v8, v4, -v9
	v_fmac_f32_e32 v10, v8, v1
	v_add_f32_e32 v11, v9, v10
	v_sub_f32_e32 v12, v7, v11
	v_sub_f32_e32 v7, v7, v12
	v_sub_f32_e32 v9, v11, v9
	v_sub_f32_e32 v7, v7, v11
	v_add_f32_e32 v5, v5, v7
	v_sub_f32_e32 v7, v9, v10
	v_add_f32_e32 v5, v7, v5
	v_add_f32_e32 v7, v12, v5
	v_mul_f32_e32 v9, v6, v7
	v_mul_f32_e32 v10, v4, v9
	v_fma_f32 v4, v9, v4, -v10
	v_fmac_f32_e32 v4, v9, v1
	v_sub_f32_e32 v1, v12, v7
	v_add_f32_e32 v1, v5, v1
	v_add_f32_e32 v5, v10, v4
	v_sub_f32_e32 v11, v7, v5
	v_sub_f32_e32 v7, v7, v11
	v_sub_f32_e32 v10, v5, v10
	v_sub_f32_e32 v5, v7, v5
	v_add_f32_e32 v1, v1, v5
	v_sub_f32_e32 v4, v10, v4
	v_add_f32_e32 v1, v4, v1
	v_add_f32_e32 v4, v8, v9
	v_add_f32_e32 v1, v11, v1
	v_sub_f32_e32 v5, v4, v8
	v_mul_f32_e32 v1, v6, v1
	v_sub_f32_e32 v5, v9, v5
	v_add_f32_e32 v1, v5, v1
	v_mul_f32_e32 v8, 0x3f317218, v0
	v_add_f32_e32 v5, v4, v1
	v_fma_f32 v9, v0, s36, -v8
	v_mul_f32_e32 v6, v5, v5
	v_fmac_f32_e32 v9, 0xb102e308, v0
	v_sub_f32_e32 v0, v5, v4
	v_fmamk_f32 v7, v6, 0x3e9b6dac, v250
	v_sub_f32_e32 v0, v1, v0
	v_add_f32_e32 v1, v8, v9
	v_fmaak_f32 v7, v6, v7, 0x3f2aaada
	v_sub_f32_e32 v4, v1, v8
	v_ldexp_f32 v8, v5, 1
	v_mul_f32_e32 v5, v5, v6
	v_mul_f32_e32 v5, v5, v7
	v_add_f32_e32 v6, v8, v5
	v_sub_f32_e32 v7, v6, v8
	v_ldexp_f32 v0, v0, 1
	v_sub_f32_e32 v5, v5, v7
	v_add_f32_e32 v0, v0, v5
	v_add_f32_e32 v5, v6, v0
	v_sub_f32_e32 v6, v5, v6
	v_sub_f32_e32 v0, v0, v6
	v_add_f32_e32 v6, v1, v5
	v_sub_f32_e32 v7, v6, v1
	v_sub_f32_e32 v8, v6, v7
	v_sub_f32_e32 v4, v9, v4
	v_sub_f32_e32 v1, v1, v8
	v_sub_f32_e32 v5, v5, v7
	v_add_f32_e32 v1, v5, v1
	v_add_f32_e32 v5, v4, v0
	v_sub_f32_e32 v7, v5, v4
	v_sub_f32_e32 v8, v5, v7
	v_sub_f32_e32 v4, v4, v8
	v_sub_f32_e32 v0, v0, v7
	v_add_f32_e32 v1, v5, v1
	v_add_f32_e32 v0, v0, v4
	v_add_f32_e32 v4, v6, v1
	v_sub_f32_e32 v5, v4, v6
	v_sub_f32_e32 v1, v1, v5
	v_add_f32_e32 v0, v0, v1
	s_mov_b32 s36, 0x7f800000
	v_add_f32_e32 v0, v4, v0
	v_cmp_neq_f32_e32 vcc, s36, v3
	v_mov_b32_e32 v1, 0x7fc00000
	s_mov_b32 s36, 0x33800000
	v_cndmask_b32_e32 v0, v251, v0, vcc
	v_cmp_ngt_f32_e32 vcc, -1.0, v3
	s_nop 1
	v_cndmask_b32_e32 v0, v1, v0, vcc
	v_cmp_neq_f32_e32 vcc, -1.0, v3
	s_waitcnt vmcnt(0)
	v_mul_f32_e32 v1, 0x3fb8aa3b, v255
	v_exp_f32_e32 v1, v1
	v_cndmask_b32_e32 v0, v230, v0, vcc
	v_cmp_lt_f32_e64 vcc, |v3|, s36
	s_nop 1
	v_cndmask_b32_e32 v0, v0, v3, vcc
	v_add_f32_e32 v0, v2, v0
	v_mul_f32_e64 v2, v0, -v1
	ds_bpermute_b32 v3, v180, v2
	s_waitcnt lgkmcnt(0)
	v_fma_f32 v1, v0, -v1, v3
	v_cndmask_b32_e64 v1, v1, v2, s[0:1]
	ds_bpermute_b32 v2, v181, v1
	s_waitcnt lgkmcnt(0)
	v_add_f32_e32 v2, v1, v2
	v_cndmask_b32_e64 v1, v2, v1, s[2:3]
	ds_bpermute_b32 v2, v182, v1
	s_waitcnt lgkmcnt(0)
	v_add_f32_e32 v2, v1, v2
	v_cndmask_b32_e64 v1, v2, v1, s[4:5]
	ds_bpermute_b32 v2, v183, v1
	s_waitcnt lgkmcnt(0)
	v_add_f32_e32 v2, v1, v2
	v_cndmask_b32_e64 v1, v2, v1, s[6:7]
	ds_bpermute_b32 v2, v184, v1
	s_waitcnt lgkmcnt(0)
	v_add_f32_e32 v2, v1, v2
	v_cndmask_b32_e64 v1, v2, v1, s[8:9]
	ds_bpermute_b32 v2, v185, v1
	s_waitcnt lgkmcnt(0)
	v_add_f32_e32 v2, v1, v2
	v_cndmask_b32_e64 v1, v2, v1, s[10:11]
	ds_write2st64_b32 v186, v1, v0 offset1:8
	s_waitcnt lgkmcnt(0)
	s_barrier
	s_and_saveexec_b64 s[36:37], s[12:13]
	s_cbranch_execz .LBB0_493
	v_mov_b32_e32 v198, 0
	s_and_saveexec_b64 s[38:39], s[14:15]
	ds_read_b32 v198, v187 offset:252
	s_or_b64 exec, exec, s[38:39]
	s_load_dwordx4 s[40:43], s[24:25], 0x60
	s_and_b32 s57, s56, 0x7c0
	s_add_i32 s58, s56, -3
	v_lshlrev_b32_e32 v208, 2, v84
	s_waitcnt lgkmcnt(0)
	s_add_u32 s38, s40, s51
	s_addc_u32 s39, s41, s23
	v_lshl_add_u64 v[152:153], s[38:39], 0, v[208:209]
	s_mov_b64 s[38:39], 0x1800
	v_lshl_add_u64 v[154:155], v[152:153], 0, s[38:39]
	s_mov_b64 s[38:39], 0x2400
	v_lshl_add_u64 v[156:157], v[152:153], 0, s[38:39]
	s_add_u32 s38, s42, s53
	s_addc_u32 s39, s43, s52
	v_lshl_add_u64 v[158:159], s[38:39], 0, v[208:209]
	s_mov_b32 s40, 0
	s_mov_b64 s[38:39], -1
	s_branch .LBB0_423

.LBB0_833:
	s_or_b64 exec, exec, vcc
	s_lshl_b32 s12, s21, 3
	s_add_i32 s12, s12, s90
	s_ashr_i32 s13, s12, 31
	s_lshl_b64 s[12:13], s[12:13], 13
	v_cvt_pk_bf16_f32 v88, v50, v49
	v_lshl_add_u64 v[50:51], v[128:129], 0, s[12:13]
	v_mov_b32_e32 v131, v209
	v_cvt_pk_bf16_f32 v92, v16, v17
	v_cvt_pk_bf16_f32 v100, v0, v1
	v_cvt_pk_bf16_f32 v89, v33, v32
	v_mov_b32_e32 v32, v209
	v_mov_b32_e32 v64, v209
	v_mov_b32_e32 v0, v209
	v_mov_b32_e32 v16, v209
	s_waitcnt lgkmcnt(0)
	v_lshl_add_u64 v[48:49], v[50:51], 0, v[208:209]
	v_lshl_add_u64 v[50:51], v[50:51], 0, v[130:131]
	global_load_dwordx4 v[52:55], v[48:49], off
	global_load_dwordx4 v[56:59], v[50:51], off
	global_load_dwordx4 v[226:229], v[48:49], off offset:32
	global_load_dwordx4 v[232:235], v[50:51], off offset:32
	global_load_dwordx4 v[236:239], v[48:49], off offset:64
	global_load_dwordx4 v[240:243], v[50:51], off offset:64
	global_load_dwordx4 v[244:247], v[48:49], off offset:96
	s_nop 0
	global_load_dwordx4 v[48:51], v[50:51], off offset:96
	ds_read_b128 v[60:63], v193 offset:22528
	ds_read_b128 v[202:205], v193 offset:22560
	v_cvt_pk_bf16_f32 v90, v35, v34
	v_cvt_pk_bf16_f32 v91, v37, v36
	v_cvt_pk_bf16_f32 v80, v39, v38
	v_cvt_pk_bf16_f32 v81, v41, v40
	v_cvt_pk_bf16_f32 v82, v43, v42
	v_cvt_pk_bf16_f32 v83, v45, v44
	v_mov_b32_e32 v33, v32
	v_mov_b32_e32 v34, v32
	v_mov_b32_e32 v35, v32
	v_mov_b32_e32 v36, v32
	v_mov_b32_e32 v37, v32
	v_mov_b32_e32 v38, v32
	v_mov_b32_e32 v39, v32
	v_mov_b32_e32 v40, v32
	v_mov_b32_e32 v41, v32
	v_mov_b32_e32 v42, v32
	v_mov_b32_e32 v43, v32
	v_mov_b32_e32 v44, v32
	v_mov_b32_e32 v45, v32
	v_mov_b32_e32 v46, v32
	v_mov_b32_e32 v47, v32
	v_mov_b32_e32 v65, v64
	v_mov_b32_e32 v66, v64
	v_mov_b32_e32 v67, v64
	v_mov_b32_e32 v68, v64
	v_mov_b32_e32 v69, v64
	v_mov_b32_e32 v70, v64
	v_mov_b32_e32 v71, v64
	v_mov_b32_e32 v72, v64
	v_mov_b32_e32 v73, v64
	v_mov_b32_e32 v74, v64
	v_mov_b32_e32 v75, v64
	v_mov_b32_e32 v76, v64
	v_mov_b32_e32 v77, v64
	v_mov_b32_e32 v78, v64
	v_mov_b32_e32 v79, v64
	v_cvt_pk_bf16_f32 v93, v18, v19
	v_cvt_pk_bf16_f32 v94, v20, v21
	v_cvt_pk_bf16_f32 v95, v22, v23
	v_cvt_pk_bf16_f32 v84, v24, v25
	v_cvt_pk_bf16_f32 v85, v26, v27
	v_cvt_pk_bf16_f32 v86, v28, v29
	v_cvt_pk_bf16_f32 v87, v30, v31
	v_cvt_pk_bf16_f32 v101, v2, v3
	v_cvt_pk_bf16_f32 v102, v4, v5
	v_cvt_pk_bf16_f32 v103, v6, v7
	v_cvt_pk_bf16_f32 v96, v8, v9
	v_cvt_pk_bf16_f32 v97, v10, v11
	v_cvt_pk_bf16_f32 v98, v12, v13
	v_cvt_pk_bf16_f32 v99, v14, v15
	v_mov_b32_e32 v1, v0
	v_mov_b32_e32 v2, v0
	v_mov_b32_e32 v3, v0
	v_mov_b32_e32 v4, v0
	v_mov_b32_e32 v5, v0
	v_mov_b32_e32 v6, v0
	v_mov_b32_e32 v7, v0
	v_mov_b32_e32 v8, v0
	v_mov_b32_e32 v9, v0
	v_mov_b32_e32 v10, v0
	v_mov_b32_e32 v11, v0
	v_mov_b32_e32 v12, v0
	v_mov_b32_e32 v13, v0
	s_waitcnt vmcnt(7) lgkmcnt(1)
	v_mfma_f32_32x32x16_bf16 v[32:47], v[60:63], v[52:55], v[32:47]
	v_mov_b32_e32 v14, v0
	v_mov_b32_e32 v15, v0
	v_mov_b32_e32 v17, v16
	v_mov_b32_e32 v18, v16
	v_mov_b32_e32 v19, v16
	v_mov_b32_e32 v20, v16
	v_mov_b32_e32 v21, v16
	s_waitcnt vmcnt(6)
	v_mfma_f32_32x32x16_bf16 v[64:79], v[60:63], v[56:59], v[64:79]
	ds_read_b128 v[60:63], v194 offset:22528
	ds_read_b128 v[210:213], v194 offset:22560
	v_mov_b32_e32 v22, v16
	v_mov_b32_e32 v23, v16
	v_mov_b32_e32 v24, v16
	v_mov_b32_e32 v25, v16
	v_mov_b32_e32 v26, v16
	v_mov_b32_e32 v27, v16
	v_mov_b32_e32 v28, v16
	v_mov_b32_e32 v29, v16
	v_mov_b32_e32 v30, v16
	v_mov_b32_e32 v31, v16
	s_waitcnt lgkmcnt(1)
	v_mfma_f32_32x32x16_bf16 v[0:15], v[60:63], v[52:55], v[0:15]
	v_mfma_f32_32x32x16_bf16 v[16:31], v[60:63], v[56:59], v[16:31]
	ds_read_b128 v[60:63], v194 offset:22592
	s_waitcnt vmcnt(5)
	v_mfma_f32_32x32x16_bf16 v[32:47], v[202:205], v[226:229], v[32:47]
	s_waitcnt vmcnt(4)
	v_mfma_f32_32x32x16_bf16 v[64:79], v[202:205], v[232:235], v[64:79]
	s_waitcnt lgkmcnt(1)
	v_mfma_f32_32x32x16_bf16 v[16:31], v[210:213], v[232:235], v[16:31]
	v_mfma_f32_32x32x16_bf16 v[0:15], v[210:213], v[226:229], v[0:15]
	ds_read_b128 v[52:55], v193 offset:22592
	s_waitcnt vmcnt(3) lgkmcnt(0)
	v_mfma_f32_32x32x16_bf16 v[32:47], v[52:55], v[236:239], v[32:47]
	v_mfma_f32_32x32x16_bf16 v[0:15], v[60:63], v[236:239], v[0:15]
	s_waitcnt vmcnt(2)
	v_mfma_f32_32x32x16_bf16 v[64:79], v[52:55], v[240:243], v[64:79]
	ds_read_b128 v[52:55], v193 offset:22624
	v_mfma_f32_32x32x16_bf16 v[16:31], v[60:63], v[240:243], v[16:31]
	ds_read_b128 v[60:63], v194 offset:22624
	s_waitcnt vmcnt(1) lgkmcnt(1)
	v_mfma_f32_32x32x16_bf16 v[32:47], v[52:55], v[244:247], v[32:47]
	s_waitcnt vmcnt(0)
	v_mfma_f32_32x32x16_bf16 v[64:79], v[52:55], v[48:51], v[64:79]
	s_waitcnt lgkmcnt(0)
	v_mfma_f32_32x32x16_bf16 v[16:31], v[60:63], v[48:51], v[16:31]
	ds_read_b128 v[48:51], v154
	ds_read_b128 v[52:55], v154 offset:32
	s_waitcnt lgkmcnt(1)
	v_mul_f32_e32 v48, 0x3fb8aa3b, v48
	v_exp_f32_e32 v202, v48
	v_mul_f32_e32 v48, 0x3fb8aa3b, v49
	v_exp_f32_e32 v203, v48
	v_mul_f32_e32 v48, 0x3fb8aa3b, v50
	v_exp_f32_e32 v204, v48
	v_mul_f32_e32 v48, 0x3fb8aa3b, v51
	v_exp_f32_e32 v205, v48
	s_waitcnt lgkmcnt(0)
	v_mul_f32_e32 v48, 0x3fb8aa3b, v52
	v_exp_f32_e32 v206, v48
	v_mul_f32_e32 v48, 0x3fb8aa3b, v53
	v_exp_f32_e32 v207, v48
	v_mul_f32_e32 v48, 0x3fb8aa3b, v54
	v_exp_f32_e32 v210, v48
	v_mul_f32_e32 v48, 0x3fb8aa3b, v55
	v_exp_f32_e32 v211, v48
	ds_read_b128 v[48:51], v154 offset:64
	v_pk_mul_f32 v[52:53], v[36:37], v[206:207]
	v_pk_mul_f32 v[36:37], v[68:69], v[206:207]
	v_pk_mul_f32 v[54:55], v[38:39], v[210:211]
	v_pk_mul_f32 v[38:39], v[70:71], v[210:211]
	s_waitcnt lgkmcnt(0)
	v_mul_f32_e32 v48, 0x3fb8aa3b, v48
	v_exp_f32_e32 v212, v48
	v_mul_f32_e32 v48, 0x3fb8aa3b, v49
	v_exp_f32_e32 v213, v48
	v_mul_f32_e32 v48, 0x3fb8aa3b, v50
	v_exp_f32_e32 v214, v48
	v_mul_f32_e32 v48, 0x3fb8aa3b, v51
	v_exp_f32_e32 v215, v48
	ds_read_b128 v[48:51], v154 offset:96
	v_mfma_f32_32x32x16_bf16 v[0:15], v[60:63], v[244:247], v[0:15]
	v_mul_f32_e64 v56, v40, v212
	v_mul_f32_e64 v57, v41, v213
	v_mul_f32_e64 v40, v72, v212
	v_mul_f32_e64 v41, v73, v213
	v_mul_f32_e64 v58, v42, v214
	v_mul_f32_e64 v59, v43, v215
	s_waitcnt lgkmcnt(0)
	v_mul_f32_e32 v48, 0x3fb8aa3b, v48
	v_exp_f32_e32 v216, v48
	v_mul_f32_e32 v48, 0x3fb8aa3b, v49
	v_exp_f32_e32 v217, v48
	v_mul_f32_e32 v48, 0x3fb8aa3b, v50
	v_exp_f32_e32 v218, v48
	v_mul_f32_e32 v48, 0x3fb8aa3b, v51
	v_exp_f32_e32 v219, v48
	v_pk_mul_f32 v[50:51], v[34:35], v[204:205]
	v_pk_mul_f32 v[48:49], v[32:33], v[202:203]
	v_pk_mul_f32 v[34:35], v[66:67], v[204:205]
	v_pk_mul_f32 v[32:33], v[64:65], v[202:203]
	ds_read_b128 v[64:67], v154 offset:128
	v_pk_mul_f32 v[42:43], v[74:75], v[214:215]
	v_pk_mul_f32 v[60:61], v[44:45], v[216:217]
	v_pk_mul_f32 v[44:45], v[76:77], v[216:217]
	v_pk_mul_f32 v[62:63], v[46:47], v[218:219]
	s_waitcnt lgkmcnt(0)
	v_mul_f32_e32 v64, 0x3fb8aa3b, v64
	v_exp_f32_e32 v68, v64
	v_mul_f32_e32 v64, 0x3fb8aa3b, v65
	v_exp_f32_e32 v69, v64
	v_mul_f32_e32 v64, 0x3fb8aa3b, v66
	v_exp_f32_e32 v70, v64
	v_mul_f32_e32 v64, 0x3fb8aa3b, v67
	v_exp_f32_e32 v71, v64
	ds_read_b128 v[64:67], v154 offset:160
	v_pk_mul_f32 v[46:47], v[78:79], v[218:219]
	v_pk_mul_f32 v[0:1], v[0:1], v[68:69]
	v_pk_mul_f32 v[2:3], v[2:3], v[70:71]
	v_pk_mul_f32 v[18:19], v[18:19], v[70:71]
	s_waitcnt lgkmcnt(0)
	v_mul_f32_e32 v64, 0x3fb8aa3b, v64
	v_exp_f32_e32 v72, v64
	v_mul_f32_e32 v64, 0x3fb8aa3b, v65
	v_exp_f32_e32 v73, v64
	v_mul_f32_e32 v64, 0x3fb8aa3b, v66
	v_exp_f32_e32 v74, v64
	v_mul_f32_e32 v64, 0x3fb8aa3b, v67
	v_exp_f32_e32 v75, v64
	ds_read_b128 v[64:67], v154 offset:192
	v_pk_mul_f32 v[4:5], v[4:5], v[72:73]
	v_pk_mul_f32 v[16:17], v[16:17], v[68:69]
	v_pk_mul_f32 v[6:7], v[6:7], v[74:75]
	v_pk_mul_f32 v[22:23], v[22:23], v[74:75]
	s_waitcnt lgkmcnt(0)
	v_mul_f32_e32 v64, 0x3fb8aa3b, v64
	v_exp_f32_e32 v76, v64
	v_mul_f32_e32 v64, 0x3fb8aa3b, v65
	v_exp_f32_e32 v77, v64
	v_mul_f32_e32 v64, 0x3fb8aa3b, v66
	v_exp_f32_e32 v78, v64
	v_mul_f32_e32 v64, 0x3fb8aa3b, v67
	v_exp_f32_e32 v79, v64
	ds_read_b128 v[64:67], v154 offset:224
	v_pk_mul_f32 v[8:9], v[8:9], v[76:77]
	v_pk_mul_f32 v[20:21], v[20:21], v[72:73]
	v_pk_mul_f32 v[10:11], v[10:11], v[78:79]
	v_pk_mul_f32 v[26:27], v[26:27], v[78:79]
	s_waitcnt lgkmcnt(0)
	v_mul_f32_e32 v64, 0x3fb8aa3b, v64
	v_mul_f32_e32 v65, 0x3fb8aa3b, v65
	v_mul_f32_e32 v66, 0x3fb8aa3b, v66
	v_mul_f32_e32 v67, 0x3fb8aa3b, v67
	v_exp_f32_e32 v64, v64
	v_exp_f32_e32 v65, v65
	v_exp_f32_e32 v66, v66
	v_exp_f32_e32 v67, v67
	v_pk_mul_f32 v[24:25], v[24:25], v[76:77]
	v_pk_mul_f32 v[12:13], v[12:13], v[64:65]
	v_pk_mul_f32 v[28:29], v[28:29], v[64:65]
	v_pk_mul_f32 v[14:15], v[14:15], v[66:67]
	v_pk_mul_f32 v[30:31], v[30:31], v[66:67]
	ds_read_b64_tr_b16 v[64:65], v195 offset:40960
	ds_read_b64_tr_b16 v[66:67], v195 offset:41984
	ds_read_b64_tr_b16 v[68:69], v196 offset:40960
	ds_read_b64_tr_b16 v[70:71], v196 offset:41984
	s_waitcnt lgkmcnt(2)
	v_mfma_f32_32x32x16_bf16 v[0:15], v[92:95], v[64:67], v[0:15]
	ds_read_b64_tr_b16 v[72:73], v195 offset:43008
	ds_read_b64_tr_b16 v[74:75], v195 offset:44032
	ds_read_b64_tr_b16 v[76:77], v196 offset:43008
	ds_read_b64_tr_b16 v[78:79], v196 offset:44032
	s_waitcnt lgkmcnt(4)
	v_mfma_f32_32x32x16_bf16 v[16:31], v[92:95], v[68:71], v[16:31]
	s_waitcnt lgkmcnt(2)
	v_mfma_f32_32x32x16_bf16 v[0:15], v[84:87], v[72:75], v[0:15]
	v_mfma_f32_32x32x16_bf16 v[48:63], v[100:103], v[64:67], v[48:63]
	ds_read_b64_tr_b16 v[64:65], v195 offset:45056
	ds_read_b64_tr_b16 v[66:67], v195 offset:46080
	s_waitcnt lgkmcnt(2)
	v_mfma_f32_32x32x16_bf16 v[16:31], v[84:87], v[76:79], v[16:31]
	s_waitcnt lgkmcnt(0)
	v_mfma_f32_32x32x16_bf16 v[0:15], v[88:91], v[64:67], v[0:15]
	ds_read_b64_tr_b16 v[64:65], v196 offset:45056
	ds_read_b64_tr_b16 v[66:67], v196 offset:46080
	s_waitcnt lgkmcnt(0)
	v_mfma_f32_32x32x16_bf16 v[16:31], v[88:91], v[64:67], v[16:31]
	ds_read_b64_tr_b16 v[64:65], v195 offset:47104
	ds_read_b64_tr_b16 v[66:67], v195 offset:48128
	s_waitcnt lgkmcnt(0)
	v_mfma_f32_32x32x16_bf16 v[0:15], v[80:83], v[64:67], v[0:15]
	ds_read_b64_tr_b16 v[64:65], v196 offset:47104
	ds_read_b64_tr_b16 v[66:67], v196 offset:48128
	s_load_dwordx2 s[12:13], s[92:93], 0x80
	s_waitcnt lgkmcnt(0)
	s_add_u32 s12, s12, s4
	s_addc_u32 s13, s13, s5
	v_mfma_f32_32x32x16_bf16 v[16:31], v[80:83], v[64:67], v[16:31]
	global_load_dword v64, v209, s[12:13]
	ds_read_u16 v65, v155 offset:40960
	s_waitcnt lgkmcnt(0)
	v_lshlrev_b32_e32 v65, 16, v65
	v_mfma_f32_32x32x16_bf16 v[48:63], v[96:99], v[72:75], v[48:63]
	v_mfma_f32_32x32x16_bf16 v[32:47], v[100:103], v[68:71], v[32:47]
	s_waitcnt vmcnt(0)
	s_nop 9
	v_fma_f32 v48, v64, v65, v48
	v_mfma_f32_32x32x16_bf16 v[32:47], v[96:99], v[76:79], v[32:47]
	v_bfe_u32 v65, v48, 16, 1
	v_add3_u32 v48, v48, v65, s63
	ds_write_b16_d16_hi v155, v48 offset:40960
	ds_read_u16 v48, v155 offset:41024
	s_waitcnt lgkmcnt(0)
	v_lshlrev_b32_e32 v48, 16, v48
	s_nop 5
	v_fma_f32 v32, v64, v48, v32
	v_bfe_u32 v48, v32, 16, 1
	v_add3_u32 v32, v32, v48, s63
	ds_write_b16_d16_hi v155, v32 offset:41024
	ds_read_u16 v32, v155 offset:41088
	s_waitcnt lgkmcnt(0)
	v_lshlrev_b32_e32 v32, 16, v32
	v_fma_f32 v32, v64, v32, v49
	v_bfe_u32 v48, v32, 16, 1
	v_add3_u32 v32, v32, v48, s63
	ds_write_b16_d16_hi v155, v32 offset:41088
	ds_read_u16 v32, v155 offset:41152
	s_waitcnt lgkmcnt(0)
	v_lshlrev_b32_e32 v32, 16, v32
	v_fma_f32 v32, v64, v32, v33
	v_bfe_u32 v33, v32, 16, 1
	v_add3_u32 v32, v32, v33, s63
	ds_write_b16_d16_hi v155, v32 offset:41152
	ds_read_u16 v32, v155 offset:41280
	s_waitcnt lgkmcnt(0)
	v_lshlrev_b32_e32 v32, 16, v32
	v_fma_f32 v32, v64, v32, v50
	v_bfe_u32 v33, v32, 16, 1
	v_add3_u32 v32, v32, v33, s63
	ds_write_b16_d16_hi v155, v32 offset:41280
	ds_read_u16 v32, v155 offset:41216
	s_waitcnt lgkmcnt(0)
	v_lshlrev_b32_e32 v32, 16, v32
	v_fma_f32 v32, v64, v32, v34
	v_bfe_u32 v33, v32, 16, 1
	v_add3_u32 v32, v32, v33, s63
	ds_write_b16_d16_hi v155, v32 offset:41216
	ds_read_u16 v32, v155 offset:41408
	s_waitcnt lgkmcnt(0)
	v_lshlrev_b32_e32 v32, 16, v32
	v_fma_f32 v32, v64, v32, v51
	v_bfe_u32 v33, v32, 16, 1
	v_add3_u32 v32, v32, v33, s63
	ds_write_b16_d16_hi v155, v32 offset:41408
	ds_read_u16 v32, v155 offset:41344
	s_waitcnt lgkmcnt(0)
	v_lshlrev_b32_e32 v32, 16, v32
	v_fma_f32 v32, v64, v32, v35
	v_bfe_u32 v33, v32, 16, 1
	v_add3_u32 v32, v32, v33, s63
	ds_write_b16_d16_hi v155, v32 offset:41344
	ds_read_u16 v32, v155 offset:41984
	s_waitcnt lgkmcnt(0)
	v_lshlrev_b32_e32 v32, 16, v32
	v_fma_f32 v32, v64, v32, v52
	v_bfe_u32 v33, v32, 16, 1
	v_add3_u32 v32, v32, v33, s63
	ds_write_b16_d16_hi v155, v32 offset:41984
	ds_read_u16 v32, v155 offset:42048
	s_waitcnt lgkmcnt(0)
	v_lshlrev_b32_e32 v32, 16, v32
	v_fma_f32 v32, v64, v32, v36
	v_bfe_u32 v33, v32, 16, 1
	v_add3_u32 v32, v32, v33, s63
	ds_write_b16_d16_hi v155, v32 offset:42048
	ds_read_u16 v32, v155 offset:42112
	s_waitcnt lgkmcnt(0)
	v_lshlrev_b32_e32 v32, 16, v32
	v_fma_f32 v32, v64, v32, v53
	v_bfe_u32 v33, v32, 16, 1
	v_add3_u32 v32, v32, v33, s63
	ds_write_b16_d16_hi v155, v32 offset:42112
	ds_read_u16 v32, v155 offset:42176
	s_waitcnt lgkmcnt(0)
	v_lshlrev_b32_e32 v32, 16, v32
	v_fma_f32 v32, v64, v32, v37
	v_bfe_u32 v33, v32, 16, 1
	v_add3_u32 v32, v32, v33, s63
	ds_write_b16_d16_hi v155, v32 offset:42176
	ds_read_u16 v32, v155 offset:42304
	s_waitcnt lgkmcnt(0)
	v_lshlrev_b32_e32 v32, 16, v32
	v_fma_f32 v32, v64, v32, v54
	v_bfe_u32 v33, v32, 16, 1
	v_add3_u32 v32, v32, v33, s63
	ds_write_b16_d16_hi v155, v32 offset:42304
	ds_read_u16 v32, v155 offset:42240
	s_waitcnt lgkmcnt(0)
	v_lshlrev_b32_e32 v32, 16, v32
	v_fma_f32 v32, v64, v32, v38
	v_bfe_u32 v33, v32, 16, 1
	v_add3_u32 v32, v32, v33, s63
	ds_write_b16_d16_hi v155, v32 offset:42240
	ds_read_u16 v32, v155 offset:42432
	s_waitcnt lgkmcnt(0)
	v_lshlrev_b32_e32 v32, 16, v32
	v_fma_f32 v32, v64, v32, v55
	v_bfe_u32 v33, v32, 16, 1
	v_add3_u32 v32, v32, v33, s63
	ds_write_b16_d16_hi v155, v32 offset:42432
	ds_read_u16 v32, v155 offset:42368
	s_waitcnt lgkmcnt(0)
	v_lshlrev_b32_e32 v32, 16, v32
	v_fma_f32 v32, v64, v32, v39
	v_bfe_u32 v33, v32, 16, 1
	v_add3_u32 v32, v32, v33, s63
	ds_write_b16_d16_hi v155, v32 offset:42368
	ds_read_u16 v32, v155 offset:43008
	s_waitcnt lgkmcnt(0)
	v_lshlrev_b32_e32 v32, 16, v32
	v_fma_f32 v32, v64, v32, v56
	v_bfe_u32 v33, v32, 16, 1
	v_add3_u32 v32, v32, v33, s63
	ds_write_b16_d16_hi v155, v32 offset:43008
	ds_read_u16 v32, v155 offset:43072
	s_waitcnt lgkmcnt(0)
	v_lshlrev_b32_e32 v32, 16, v32
	v_fma_f32 v32, v64, v32, v40
	v_bfe_u32 v33, v32, 16, 1
	v_add3_u32 v32, v32, v33, s63
	ds_write_b16_d16_hi v155, v32 offset:43072
	ds_read_u16 v32, v155 offset:43136
	s_waitcnt lgkmcnt(0)
	v_lshlrev_b32_e32 v32, 16, v32
	v_fma_f32 v32, v64, v32, v57
	v_bfe_u32 v33, v32, 16, 1
	v_add3_u32 v32, v32, v33, s63
	ds_write_b16_d16_hi v155, v32 offset:43136
	ds_read_u16 v32, v155 offset:43200
	s_waitcnt lgkmcnt(0)
	v_lshlrev_b32_e32 v32, 16, v32
	v_fma_f32 v32, v64, v32, v41
	v_bfe_u32 v33, v32, 16, 1
	v_add3_u32 v32, v32, v33, s63
	ds_write_b16_d16_hi v155, v32 offset:43200
	ds_read_u16 v32, v155 offset:43328
	s_waitcnt lgkmcnt(0)
	v_lshlrev_b32_e32 v32, 16, v32
	v_fma_f32 v32, v64, v32, v58
	v_bfe_u32 v33, v32, 16, 1
	v_add3_u32 v32, v32, v33, s63
	ds_write_b16_d16_hi v155, v32 offset:43328
	ds_read_u16 v32, v155 offset:43264
	s_waitcnt lgkmcnt(0)
	v_lshlrev_b32_e32 v32, 16, v32
	v_fma_f32 v32, v64, v32, v42
	v_bfe_u32 v33, v32, 16, 1
	v_add3_u32 v32, v32, v33, s63
	ds_write_b16_d16_hi v155, v32 offset:43264
	ds_read_u16 v32, v155 offset:43456
	s_waitcnt lgkmcnt(0)
	v_lshlrev_b32_e32 v32, 16, v32
	v_fma_f32 v32, v64, v32, v59
	v_bfe_u32 v33, v32, 16, 1
	v_add3_u32 v32, v32, v33, s63
	ds_write_b16_d16_hi v155, v32 offset:43456
	ds_read_u16 v32, v155 offset:43392
	s_waitcnt lgkmcnt(0)
	v_lshlrev_b32_e32 v32, 16, v32
	v_fma_f32 v32, v64, v32, v43
	v_bfe_u32 v33, v32, 16, 1
	v_add3_u32 v32, v32, v33, s63
	ds_write_b16_d16_hi v155, v32 offset:43392
	ds_read_u16 v32, v155 offset:44032
	s_waitcnt lgkmcnt(0)
	v_lshlrev_b32_e32 v32, 16, v32
	v_fma_f32 v32, v64, v32, v60
	v_bfe_u32 v33, v32, 16, 1
	v_add3_u32 v32, v32, v33, s63
	ds_write_b16_d16_hi v155, v32 offset:44032
	ds_read_u16 v32, v155 offset:44096
	s_waitcnt lgkmcnt(0)
	v_lshlrev_b32_e32 v32, 16, v32
	v_fma_f32 v32, v64, v32, v44
	v_bfe_u32 v33, v32, 16, 1
	v_add3_u32 v32, v32, v33, s63
	ds_write_b16_d16_hi v155, v32 offset:44096
	ds_read_u16 v32, v155 offset:44160
	s_waitcnt lgkmcnt(0)
	v_lshlrev_b32_e32 v32, 16, v32
	v_fma_f32 v32, v64, v32, v61
	v_bfe_u32 v33, v32, 16, 1
	v_add3_u32 v32, v32, v33, s63
	ds_write_b16_d16_hi v155, v32 offset:44160
	ds_read_u16 v32, v155 offset:44224
	s_waitcnt lgkmcnt(0)
	v_lshlrev_b32_e32 v32, 16, v32
	v_fma_f32 v32, v64, v32, v45
	v_bfe_u32 v33, v32, 16, 1
	v_add3_u32 v32, v32, v33, s63
	ds_write_b16_d16_hi v155, v32 offset:44224
	ds_read_u16 v32, v155 offset:44352
	s_waitcnt lgkmcnt(0)
	v_lshlrev_b32_e32 v32, 16, v32
	v_fma_f32 v32, v64, v32, v62
	v_bfe_u32 v33, v32, 16, 1
	v_add3_u32 v32, v32, v33, s63
	ds_write_b16_d16_hi v155, v32 offset:44352
	ds_read_u16 v32, v155 offset:44288
	s_waitcnt lgkmcnt(0)
	v_lshlrev_b32_e32 v32, 16, v32
	v_fma_f32 v32, v64, v32, v46
	v_bfe_u32 v33, v32, 16, 1
	v_add3_u32 v32, v32, v33, s63
	ds_write_b16_d16_hi v155, v32 offset:44288
	ds_read_u16 v32, v155 offset:44480
	s_waitcnt lgkmcnt(0)
	v_lshlrev_b32_e32 v32, 16, v32
	v_fmac_f32_e32 v63, v64, v32
	v_bfe_u32 v32, v63, 16, 1
	v_add3_u32 v32, v63, v32, s63
	ds_write_b16_d16_hi v155, v32 offset:44480
	ds_read_u16 v32, v155 offset:44416
	s_waitcnt lgkmcnt(0)
	v_lshlrev_b32_e32 v32, 16, v32
	v_fmac_f32_e32 v47, v64, v32
	v_bfe_u32 v32, v47, 16, 1
	v_add3_u32 v32, v47, v32, s63
	ds_write_b16_d16_hi v155, v32 offset:44416
	ds_read_u16 v32, v155 offset:45056
	s_waitcnt lgkmcnt(0)
	v_lshlrev_b32_e32 v32, 16, v32
	v_fma_f32 v0, v64, v32, v0
	v_bfe_u32 v32, v0, 16, 1
	v_add3_u32 v0, v0, v32, s63
	ds_write_b16_d16_hi v155, v0 offset:45056
	ds_read_u16 v0, v155 offset:45120
	s_waitcnt lgkmcnt(0)
	v_lshlrev_b32_e32 v0, 16, v0
	v_fma_f32 v0, v64, v0, v16
	v_bfe_u32 v16, v0, 16, 1
	v_add3_u32 v0, v0, v16, s63
	ds_write_b16_d16_hi v155, v0 offset:45120
	ds_read_u16 v0, v155 offset:45184
	s_waitcnt lgkmcnt(0)
	v_lshlrev_b32_e32 v0, 16, v0
	v_fma_f32 v0, v64, v0, v1
	v_bfe_u32 v1, v0, 16, 1
	v_add3_u32 v0, v0, v1, s63
	ds_write_b16_d16_hi v155, v0 offset:45184
	ds_read_u16 v0, v155 offset:45248
	s_waitcnt lgkmcnt(0)
	v_lshlrev_b32_e32 v0, 16, v0
	v_fma_f32 v0, v64, v0, v17
	v_bfe_u32 v1, v0, 16, 1
	v_add3_u32 v0, v0, v1, s63
	ds_write_b16_d16_hi v155, v0 offset:45248
	ds_read_u16 v0, v155 offset:45376
	s_waitcnt lgkmcnt(0)
	v_lshlrev_b32_e32 v0, 16, v0
	v_fma_f32 v0, v64, v0, v2
	v_bfe_u32 v1, v0, 16, 1
	v_add3_u32 v0, v0, v1, s63
	ds_write_b16_d16_hi v155, v0 offset:45376
	ds_read_u16 v0, v155 offset:45312
	s_waitcnt lgkmcnt(0)
	v_lshlrev_b32_e32 v0, 16, v0
	v_fma_f32 v0, v64, v0, v18
	v_bfe_u32 v1, v0, 16, 1
	v_add3_u32 v0, v0, v1, s63
	ds_write_b16_d16_hi v155, v0 offset:45312
	ds_read_u16 v0, v155 offset:45504
	s_waitcnt lgkmcnt(0)
	v_lshlrev_b32_e32 v0, 16, v0
	v_fma_f32 v0, v64, v0, v3
	v_bfe_u32 v1, v0, 16, 1
	v_add3_u32 v0, v0, v1, s63
	ds_write_b16_d16_hi v155, v0 offset:45504
	ds_read_u16 v0, v155 offset:45440
	s_waitcnt lgkmcnt(0)
	v_lshlrev_b32_e32 v0, 16, v0
	v_fma_f32 v0, v64, v0, v19
	v_bfe_u32 v1, v0, 16, 1
	v_add3_u32 v0, v0, v1, s63
	ds_write_b16_d16_hi v155, v0 offset:45440
	ds_read_u16 v0, v155 offset:46080
	s_waitcnt lgkmcnt(0)
	v_lshlrev_b32_e32 v0, 16, v0
	v_fma_f32 v0, v64, v0, v4
	v_bfe_u32 v1, v0, 16, 1
	v_add3_u32 v0, v0, v1, s63
	ds_write_b16_d16_hi v155, v0 offset:46080
	ds_read_u16 v0, v155 offset:46144
	s_waitcnt lgkmcnt(0)
	v_lshlrev_b32_e32 v0, 16, v0
	v_fma_f32 v0, v64, v0, v20
	v_bfe_u32 v1, v0, 16, 1
	v_add3_u32 v0, v0, v1, s63
	ds_write_b16_d16_hi v155, v0 offset:46144
	ds_read_u16 v0, v155 offset:46208
	s_waitcnt lgkmcnt(0)
	v_lshlrev_b32_e32 v0, 16, v0
	v_fma_f32 v0, v64, v0, v5
	v_bfe_u32 v1, v0, 16, 1
	v_add3_u32 v0, v0, v1, s63
	ds_write_b16_d16_hi v155, v0 offset:46208
	ds_read_u16 v0, v155 offset:46272
	s_waitcnt lgkmcnt(0)
	v_lshlrev_b32_e32 v0, 16, v0
	v_fma_f32 v0, v64, v0, v21
	v_bfe_u32 v1, v0, 16, 1
	v_add3_u32 v0, v0, v1, s63
	ds_write_b16_d16_hi v155, v0 offset:46272
	ds_read_u16 v0, v155 offset:46400
	s_waitcnt lgkmcnt(0)
	v_lshlrev_b32_e32 v0, 16, v0
	v_fma_f32 v0, v64, v0, v6
	v_bfe_u32 v1, v0, 16, 1
	v_add3_u32 v0, v0, v1, s63
	ds_write_b16_d16_hi v155, v0 offset:46400
	ds_read_u16 v0, v155 offset:46336
	s_waitcnt lgkmcnt(0)
	v_lshlrev_b32_e32 v0, 16, v0
	v_fma_f32 v0, v64, v0, v22
	v_bfe_u32 v1, v0, 16, 1
	v_add3_u32 v0, v0, v1, s63
	ds_write_b16_d16_hi v155, v0 offset:46336
	ds_read_u16 v0, v155 offset:46528
	s_waitcnt lgkmcnt(0)
	v_lshlrev_b32_e32 v0, 16, v0
	v_fma_f32 v0, v64, v0, v7
	v_bfe_u32 v1, v0, 16, 1
	v_add3_u32 v0, v0, v1, s63
	ds_write_b16_d16_hi v155, v0 offset:46528
	ds_read_u16 v0, v155 offset:46464
	s_waitcnt lgkmcnt(0)
	v_lshlrev_b32_e32 v0, 16, v0
	v_fma_f32 v0, v64, v0, v23
	v_bfe_u32 v1, v0, 16, 1
	v_add3_u32 v0, v0, v1, s63
	ds_write_b16_d16_hi v155, v0 offset:46464
	ds_read_u16 v0, v155 offset:47104
	s_waitcnt lgkmcnt(0)
	v_lshlrev_b32_e32 v0, 16, v0
	v_fma_f32 v0, v64, v0, v8
	v_bfe_u32 v1, v0, 16, 1
	v_add3_u32 v0, v0, v1, s63
	ds_write_b16_d16_hi v155, v0 offset:47104
	ds_read_u16 v0, v155 offset:47168
	s_waitcnt lgkmcnt(0)
	v_lshlrev_b32_e32 v0, 16, v0
	v_fma_f32 v0, v64, v0, v24
	v_bfe_u32 v1, v0, 16, 1
	v_add3_u32 v0, v0, v1, s63
	ds_write_b16_d16_hi v155, v0 offset:47168
	ds_read_u16 v0, v155 offset:47232
	s_waitcnt lgkmcnt(0)
	v_lshlrev_b32_e32 v0, 16, v0
	v_fma_f32 v0, v64, v0, v9
	v_bfe_u32 v1, v0, 16, 1
	v_add3_u32 v0, v0, v1, s63
	ds_write_b16_d16_hi v155, v0 offset:47232
	ds_read_u16 v0, v155 offset:47296
	s_waitcnt lgkmcnt(0)
	v_lshlrev_b32_e32 v0, 16, v0
	v_fma_f32 v0, v64, v0, v25
	v_bfe_u32 v1, v0, 16, 1
	v_add3_u32 v0, v0, v1, s63
	ds_write_b16_d16_hi v155, v0 offset:47296
	ds_read_u16 v0, v155 offset:47424
	s_waitcnt lgkmcnt(0)
	v_lshlrev_b32_e32 v0, 16, v0
	v_fma_f32 v0, v64, v0, v10
	v_bfe_u32 v1, v0, 16, 1
	v_add3_u32 v0, v0, v1, s63
	ds_write_b16_d16_hi v155, v0 offset:47424
	ds_read_u16 v0, v155 offset:47360
	s_waitcnt lgkmcnt(0)
	v_lshlrev_b32_e32 v0, 16, v0
	v_fma_f32 v0, v64, v0, v26
	v_bfe_u32 v1, v0, 16, 1
	v_add3_u32 v0, v0, v1, s63
	ds_write_b16_d16_hi v155, v0 offset:47360
	ds_read_u16 v0, v155 offset:47552
	s_waitcnt lgkmcnt(0)
	v_lshlrev_b32_e32 v0, 16, v0
	v_fma_f32 v0, v64, v0, v11
	v_bfe_u32 v1, v0, 16, 1
	v_add3_u32 v0, v0, v1, s63
	ds_write_b16_d16_hi v155, v0 offset:47552
	ds_read_u16 v0, v155 offset:47488
	s_waitcnt lgkmcnt(0)
	v_lshlrev_b32_e32 v0, 16, v0
	v_fma_f32 v0, v64, v0, v27
	v_bfe_u32 v1, v0, 16, 1
	v_add3_u32 v0, v0, v1, s63
	ds_write_b16_d16_hi v155, v0 offset:47488
	ds_read_u16 v0, v155 offset:48128
	s_waitcnt lgkmcnt(0)
	v_lshlrev_b32_e32 v0, 16, v0
	v_fma_f32 v0, v64, v0, v12
	v_bfe_u32 v1, v0, 16, 1
	v_add3_u32 v0, v0, v1, s63
	ds_write_b16_d16_hi v155, v0 offset:48128
	ds_read_u16 v0, v155 offset:48192
	s_waitcnt lgkmcnt(0)
	v_lshlrev_b32_e32 v0, 16, v0
	v_fma_f32 v0, v64, v0, v28
	v_bfe_u32 v1, v0, 16, 1
	v_add3_u32 v0, v0, v1, s63
	ds_write_b16_d16_hi v155, v0 offset:48192
	ds_read_u16 v0, v155 offset:48256
	s_waitcnt lgkmcnt(0)
	v_lshlrev_b32_e32 v0, 16, v0
	v_fma_f32 v0, v64, v0, v13
	v_bfe_u32 v1, v0, 16, 1
	v_add3_u32 v0, v0, v1, s63
	ds_write_b16_d16_hi v155, v0 offset:48256
	ds_read_u16 v0, v155 offset:48320
	s_waitcnt lgkmcnt(0)
	v_lshlrev_b32_e32 v0, 16, v0
	v_fma_f32 v0, v64, v0, v29
	v_bfe_u32 v1, v0, 16, 1
	v_add3_u32 v0, v0, v1, s63
	ds_write_b16_d16_hi v155, v0 offset:48320
	ds_read_u16 v0, v155 offset:48448
	s_waitcnt lgkmcnt(0)
	v_lshlrev_b32_e32 v0, 16, v0
	v_fma_f32 v0, v64, v0, v14
	v_bfe_u32 v1, v0, 16, 1
	v_add3_u32 v0, v0, v1, s63
	ds_write_b16_d16_hi v155, v0 offset:48448
	ds_read_u16 v0, v155 offset:48384
	s_waitcnt lgkmcnt(0)
	v_lshlrev_b32_e32 v0, 16, v0
	v_fma_f32 v0, v64, v0, v30
	v_bfe_u32 v1, v0, 16, 1
	v_add3_u32 v0, v0, v1, s63
	ds_write_b16_d16_hi v155, v0 offset:48384
	ds_read_u16 v0, v155 offset:48576
	s_waitcnt lgkmcnt(0)
	v_lshlrev_b32_e32 v0, 16, v0
	v_fmac_f32_e32 v15, v64, v0
	v_bfe_u32 v0, v15, 16, 1
	v_add3_u32 v0, v15, v0, s63
	ds_write_b16_d16_hi v155, v0 offset:48576
	ds_read_u16 v0, v155 offset:48512
	s_waitcnt lgkmcnt(0)
	v_lshlrev_b32_e32 v0, 16, v0
	v_fmac_f32_e32 v31, v64, v0
	v_bfe_u32 v0, v31, 16, 1
	v_add3_u32 v0, v31, v0, s63
	ds_write_b16_d16_hi v155, v0 offset:48512
	v_mov_b64_e32 v[0:1], s[10:11]
	v_mad_u64_u32 v[0:1], s[12:13], v201, s62, v[0:1]
	v_lshl_add_u64 v[60:61], s[94:95], 1, v[0:1]
	v_add_co_u32_e32 v0, vcc, s82, v60
	s_mov_b64 s[12:13], 0x1000
	s_nop 0
	v_addc_co_u32_e32 v1, vcc, 0, v61, vcc
	v_lshl_add_u64 v[4:5], v[60:61], 0, s[12:13]
	global_load_dwordx4 v[52:55], v[0:1], off
	global_load_dwordx4 v[24:27], v[4:5], off offset:48
	global_load_dwordx4 v[40:43], v[4:5], off offset:32
	global_load_dwordx4 v[48:51], v[4:5], off offset:16
	s_nop 0
	global_load_dwordx4 v[0:3], v[4:5], off offset:112
	global_load_dwordx4 v[8:11], v[4:5], off offset:96
	global_load_dwordx4 v[16:19], v[4:5], off offset:80
	global_load_dwordx4 v[28:31], v[4:5], off offset:64
	ds_read_b128 v[64:67], v197 offset:40960
	ds_read_b128 v[56:59], v197 offset:40976
	ds_read_b128 v[44:47], v197 offset:40992
	ds_read_b128 v[36:39], v197 offset:41008
	ds_read_b128 v[32:35], v198 offset:40960
	ds_read_b128 v[20:23], v198 offset:40976
	ds_read_b128 v[12:15], v198 offset:40992
	ds_read_b128 v[4:7], v198 offset:41008
	s_waitcnt lgkmcnt(7)
	v_lshlrev_b32_e32 v62, 16, v64
	v_and_b32_e32 v63, 0xffff0000, v64
	v_lshlrev_b32_e32 v64, 16, v65
	v_and_b32_e32 v65, 0xffff0000, v65
	s_waitcnt vmcnt(7)
	v_lshlrev_b32_e32 v68, 16, v52
	v_and_b32_e32 v69, 0xffff0000, v52
	v_mul_f32_e32 v52, 0xbfb8aa3b, v68
	v_lshlrev_b32_e32 v72, 16, v54
	v_exp_f32_e32 v52, v52
	v_and_b32_e32 v73, 0xffff0000, v54
	v_mul_f32_e32 v54, 0xbfb8aa3b, v72
	v_exp_f32_e32 v54, v54
	v_add_f32_e32 v52, 1.0, v52
	v_rcp_f32_e32 v70, v52
	v_mul_f32_e32 v52, 0xbfb8aa3b, v69
	v_add_f32_e32 v54, 1.0, v54
	v_exp_f32_e32 v52, v52
	v_rcp_f32_e32 v74, v54
	v_mul_f32_e32 v54, 0xbfb8aa3b, v73
	v_exp_f32_e32 v54, v54
	v_add_f32_e32 v52, 1.0, v52
	v_rcp_f32_e32 v71, v52
	v_lshlrev_b32_e32 v52, 16, v53
	v_add_f32_e32 v54, 1.0, v54
	v_rcp_f32_e32 v75, v54
	v_and_b32_e32 v53, 0xffff0000, v53
	v_pk_mul_f32 v[68:69], v[70:71], v[68:69]
	v_mul_f32_e32 v70, 0xbfb8aa3b, v52
	v_mul_f32_e32 v71, 0xbfb8aa3b, v53
	v_lshlrev_b32_e32 v54, 16, v55
	v_and_b32_e32 v55, 0xffff0000, v55
	v_exp_f32_e32 v70, v70
	v_exp_f32_e32 v71, v71
	v_pk_mul_f32 v[72:73], v[74:75], v[72:73]
	v_mul_f32_e32 v74, 0xbfb8aa3b, v54
	v_mul_f32_e32 v75, 0xbfb8aa3b, v55
	v_exp_f32_e32 v74, v74
	v_exp_f32_e32 v75, v75
	v_add_f32_e32 v70, 1.0, v70
	v_add_f32_e32 v71, 1.0, v71
	v_rcp_f32_e32 v70, v70
	v_rcp_f32_e32 v71, v71
	v_add_f32_e32 v74, 1.0, v74
	v_add_f32_e32 v75, 1.0, v75
	v_rcp_f32_e32 v74, v74
	v_rcp_f32_e32 v75, v75
	v_pk_mul_f32 v[52:53], v[70:71], v[52:53]
	v_pk_mul_f32 v[68:69], v[68:69], v[62:63]
	v_pk_mul_f32 v[70:71], v[52:53], v[64:65]
	v_lshlrev_b32_e32 v64, 16, v66
	v_and_b32_e32 v65, 0xffff0000, v66
	v_lshlrev_b32_e32 v66, 16, v67
	v_and_b32_e32 v67, 0xffff0000, v67
	v_pk_mul_f32 v[54:55], v[74:75], v[54:55]
	v_pk_mul_f32 v[72:73], v[72:73], v[64:65]
	v_pk_mul_f32 v[74:75], v[54:55], v[66:67]
	v_pk_mul_f32 v[62:63], v[68:69], v[68:69]
	v_cvt_pk_bf16_f32 v66, v68, v69
	v_cvt_pk_bf16_f32 v67, v70, v71
	v_cvt_pk_bf16_f32 v68, v72, v73
	v_cvt_pk_bf16_f32 v69, v74, v75
	global_store_dwordx4 v[60:61], v[66:69], off offset:2048
	v_pk_mul_f32 v[64:65], v[72:73], v[72:73]
	s_waitcnt vmcnt(5)
	v_lshlrev_b32_e32 v72, 16, v50
	v_lshlrev_b32_e32 v68, 16, v48
	v_and_b32_e32 v69, 0xffff0000, v48
	v_mul_f32_e32 v48, 0xbfb8aa3b, v68
	v_exp_f32_e32 v48, v48
	v_and_b32_e32 v73, 0xffff0000, v50
	v_mul_f32_e32 v50, 0xbfb8aa3b, v72
	v_exp_f32_e32 v50, v50
	v_add_f32_e32 v48, 1.0, v48
	v_pk_mul_f32 v[52:53], v[70:71], v[70:71]
	v_rcp_f32_e32 v70, v48
	v_mul_f32_e32 v48, 0xbfb8aa3b, v69
	v_add_f32_e32 v50, 1.0, v50
	v_pk_mul_f32 v[54:55], v[74:75], v[74:75]
	v_exp_f32_e32 v48, v48
	v_rcp_f32_e32 v74, v50
	v_mul_f32_e32 v50, 0xbfb8aa3b, v73
	v_exp_f32_e32 v50, v50
	v_add_f32_e32 v48, 1.0, v48
	v_rcp_f32_e32 v71, v48
	v_lshlrev_b32_e32 v48, 16, v49
	v_add_f32_e32 v50, 1.0, v50
	v_rcp_f32_e32 v75, v50
	v_and_b32_e32 v49, 0xffff0000, v49
	v_pk_mul_f32 v[68:69], v[70:71], v[68:69]
	v_mul_f32_e32 v70, 0xbfb8aa3b, v48
	v_mul_f32_e32 v71, 0xbfb8aa3b, v49
	v_lshlrev_b32_e32 v50, 16, v51
	v_and_b32_e32 v51, 0xffff0000, v51
	v_exp_f32_e32 v70, v70
	v_exp_f32_e32 v71, v71
	v_pk_mul_f32 v[72:73], v[74:75], v[72:73]
	v_mul_f32_e32 v74, 0xbfb8aa3b, v50
	v_mul_f32_e32 v75, 0xbfb8aa3b, v51
	v_exp_f32_e32 v74, v74
	v_exp_f32_e32 v75, v75
	v_add_f32_e32 v70, 1.0, v70
	v_add_f32_e32 v71, 1.0, v71
	v_rcp_f32_e32 v70, v70
	v_rcp_f32_e32 v71, v71
	v_add_f32_e32 v74, 1.0, v74
	v_add_f32_e32 v75, 1.0, v75
	v_rcp_f32_e32 v74, v74
	v_rcp_f32_e32 v75, v75
	s_waitcnt lgkmcnt(6)
	v_lshlrev_b32_e32 v66, 16, v56
	v_and_b32_e32 v67, 0xffff0000, v56
	v_lshlrev_b32_e32 v56, 16, v57
	v_and_b32_e32 v57, 0xffff0000, v57
	v_pk_mul_f32 v[48:49], v[70:71], v[48:49]
	v_pk_mul_f32 v[50:51], v[74:75], v[50:51]
	v_pk_mul_f32 v[70:71], v[48:49], v[56:57]
	v_lshlrev_b32_e32 v56, 16, v58
	v_and_b32_e32 v57, 0xffff0000, v58
	v_lshlrev_b32_e32 v58, 16, v59
	v_and_b32_e32 v59, 0xffff0000, v59
	v_pk_mul_f32 v[68:69], v[68:69], v[66:67]
	v_pk_mul_f32 v[72:73], v[72:73], v[56:57]
	v_pk_mul_f32 v[58:59], v[50:51], v[58:59]
	v_pk_mul_f32 v[66:67], v[68:69], v[68:69]
	v_pk_mul_f32 v[48:49], v[70:71], v[70:71]
	v_cvt_pk_bf16_f32 v68, v68, v69
	v_cvt_pk_bf16_f32 v69, v70, v71
	v_cvt_pk_bf16_f32 v70, v72, v73
	v_cvt_pk_bf16_f32 v71, v58, v59
	global_store_dwordx4 v[60:61], v[68:71], off offset:2064
	v_pk_mul_f32 v[56:57], v[72:73], v[72:73]
	v_lshlrev_b32_e32 v72, 16, v42
	v_lshlrev_b32_e32 v68, 16, v40
	v_and_b32_e32 v69, 0xffff0000, v40
	v_mul_f32_e32 v40, 0xbfb8aa3b, v68
	v_exp_f32_e32 v40, v40
	v_and_b32_e32 v73, 0xffff0000, v42
	v_mul_f32_e32 v42, 0xbfb8aa3b, v72
	v_exp_f32_e32 v42, v42
	v_add_f32_e32 v40, 1.0, v40
	v_rcp_f32_e32 v70, v40
	v_mul_f32_e32 v40, 0xbfb8aa3b, v69
	v_add_f32_e32 v42, 1.0, v42
	v_exp_f32_e32 v40, v40
	v_rcp_f32_e32 v74, v42
	v_mul_f32_e32 v42, 0xbfb8aa3b, v73
	v_exp_f32_e32 v42, v42
	v_add_f32_e32 v40, 1.0, v40
	v_rcp_f32_e32 v71, v40
	v_lshlrev_b32_e32 v40, 16, v41
	v_add_f32_e32 v42, 1.0, v42
	v_rcp_f32_e32 v75, v42
	v_and_b32_e32 v41, 0xffff0000, v41
	v_pk_mul_f32 v[68:69], v[70:71], v[68:69]
	v_mul_f32_e32 v70, 0xbfb8aa3b, v40
	v_mul_f32_e32 v71, 0xbfb8aa3b, v41
	v_lshlrev_b32_e32 v42, 16, v43
	v_and_b32_e32 v43, 0xffff0000, v43
	v_exp_f32_e32 v70, v70
	v_exp_f32_e32 v71, v71
	v_pk_mul_f32 v[72:73], v[74:75], v[72:73]
	v_mul_f32_e32 v74, 0xbfb8aa3b, v42
	v_mul_f32_e32 v75, 0xbfb8aa3b, v43
	v_exp_f32_e32 v74, v74
	v_exp_f32_e32 v75, v75
	v_add_f32_e32 v70, 1.0, v70
	v_add_f32_e32 v71, 1.0, v71
	v_rcp_f32_e32 v70, v70
	v_rcp_f32_e32 v71, v71
	v_add_f32_e32 v74, 1.0, v74
	v_add_f32_e32 v75, 1.0, v75
	v_rcp_f32_e32 v74, v74
	v_rcp_f32_e32 v75, v75
	v_pk_mul_f32 v[50:51], v[58:59], v[58:59]
	s_waitcnt lgkmcnt(5)
	v_lshlrev_b32_e32 v58, 16, v44
	v_and_b32_e32 v59, 0xffff0000, v44
	v_lshlrev_b32_e32 v44, 16, v45
	v_and_b32_e32 v45, 0xffff0000, v45
	v_pk_mul_f32 v[40:41], v[70:71], v[40:41]
	v_pk_mul_f32 v[42:43], v[74:75], v[42:43]
	v_pk_mul_f32 v[70:71], v[40:41], v[44:45]
	v_lshlrev_b32_e32 v44, 16, v46
	v_and_b32_e32 v45, 0xffff0000, v46
	v_lshlrev_b32_e32 v46, 16, v47
	v_and_b32_e32 v47, 0xffff0000, v47
	v_pk_mul_f32 v[68:69], v[68:69], v[58:59]
	v_pk_mul_f32 v[72:73], v[72:73], v[44:45]
	v_pk_mul_f32 v[46:47], v[42:43], v[46:47]
	v_pk_mul_f32 v[58:59], v[68:69], v[68:69]
	v_pk_mul_f32 v[40:41], v[70:71], v[70:71]
	v_cvt_pk_bf16_f32 v68, v68, v69
	v_cvt_pk_bf16_f32 v69, v70, v71
	v_cvt_pk_bf16_f32 v70, v72, v73
	v_cvt_pk_bf16_f32 v71, v46, v47
	global_store_dwordx4 v[60:61], v[68:71], off offset:2080
	v_pk_mul_f32 v[44:45], v[72:73], v[72:73]
	v_lshlrev_b32_e32 v72, 16, v26
	v_lshlrev_b32_e32 v68, 16, v24
	v_and_b32_e32 v69, 0xffff0000, v24
	v_mul_f32_e32 v24, 0xbfb8aa3b, v68
	v_exp_f32_e32 v24, v24
	v_and_b32_e32 v73, 0xffff0000, v26
	v_mul_f32_e32 v26, 0xbfb8aa3b, v72
	v_exp_f32_e32 v26, v26
	v_add_f32_e32 v24, 1.0, v24
	v_rcp_f32_e32 v70, v24
	v_mul_f32_e32 v24, 0xbfb8aa3b, v69
	v_add_f32_e32 v26, 1.0, v26
	v_exp_f32_e32 v24, v24
	v_rcp_f32_e32 v74, v26
	v_mul_f32_e32 v26, 0xbfb8aa3b, v73
	v_exp_f32_e32 v26, v26
	v_add_f32_e32 v24, 1.0, v24
	v_rcp_f32_e32 v71, v24
	v_lshlrev_b32_e32 v24, 16, v25
	v_add_f32_e32 v26, 1.0, v26
	v_rcp_f32_e32 v75, v26
	v_and_b32_e32 v25, 0xffff0000, v25
	v_pk_mul_f32 v[68:69], v[70:71], v[68:69]
	v_mul_f32_e32 v70, 0xbfb8aa3b, v24
	v_mul_f32_e32 v71, 0xbfb8aa3b, v25
	v_lshlrev_b32_e32 v26, 16, v27
	v_and_b32_e32 v27, 0xffff0000, v27
	v_exp_f32_e32 v70, v70
	v_exp_f32_e32 v71, v71
	v_pk_mul_f32 v[72:73], v[74:75], v[72:73]
	v_mul_f32_e32 v74, 0xbfb8aa3b, v26
	v_mul_f32_e32 v75, 0xbfb8aa3b, v27
	v_exp_f32_e32 v74, v74
	v_exp_f32_e32 v75, v75
	v_add_f32_e32 v70, 1.0, v70
	v_add_f32_e32 v71, 1.0, v71
	v_rcp_f32_e32 v70, v70
	v_rcp_f32_e32 v71, v71
	v_add_f32_e32 v74, 1.0, v74
	v_add_f32_e32 v75, 1.0, v75
	v_rcp_f32_e32 v74, v74
	v_rcp_f32_e32 v75, v75
	v_pk_mul_f32 v[42:43], v[46:47], v[46:47]
	s_waitcnt lgkmcnt(4)
	v_lshlrev_b32_e32 v46, 16, v36
	v_and_b32_e32 v47, 0xffff0000, v36
	v_lshlrev_b32_e32 v36, 16, v37
	v_and_b32_e32 v37, 0xffff0000, v37
	v_pk_mul_f32 v[24:25], v[70:71], v[24:25]
	v_pk_mul_f32 v[26:27], v[74:75], v[26:27]
	v_pk_mul_f32 v[70:71], v[24:25], v[36:37]
	v_lshlrev_b32_e32 v36, 16, v38
	v_and_b32_e32 v37, 0xffff0000, v38
	v_lshlrev_b32_e32 v38, 16, v39
	v_and_b32_e32 v39, 0xffff0000, v39
	v_pk_mul_f32 v[68:69], v[68:69], v[46:47]
	v_pk_mul_f32 v[72:73], v[72:73], v[36:37]
	v_pk_mul_f32 v[38:39], v[26:27], v[38:39]
	v_pk_mul_f32 v[46:47], v[68:69], v[68:69]
	v_pk_mul_f32 v[24:25], v[70:71], v[70:71]
	v_cvt_pk_bf16_f32 v68, v68, v69
	v_cvt_pk_bf16_f32 v69, v70, v71
	v_cvt_pk_bf16_f32 v70, v72, v73
	v_cvt_pk_bf16_f32 v71, v38, v39
	global_store_dwordx4 v[60:61], v[68:71], off offset:2096
	v_pk_mul_f32 v[36:37], v[72:73], v[72:73]
	s_waitcnt vmcnt(4)
	v_lshlrev_b32_e32 v72, 16, v30
	v_lshlrev_b32_e32 v68, 16, v28
	v_and_b32_e32 v69, 0xffff0000, v28
	v_mul_f32_e32 v28, 0xbfb8aa3b, v68
	v_exp_f32_e32 v28, v28
	v_and_b32_e32 v73, 0xffff0000, v30
	v_mul_f32_e32 v30, 0xbfb8aa3b, v72
	v_exp_f32_e32 v30, v30
	v_add_f32_e32 v28, 1.0, v28
	v_rcp_f32_e32 v70, v28
	v_mul_f32_e32 v28, 0xbfb8aa3b, v69
	v_add_f32_e32 v30, 1.0, v30
	v_exp_f32_e32 v28, v28
	v_rcp_f32_e32 v74, v30
	v_mul_f32_e32 v30, 0xbfb8aa3b, v73
	v_exp_f32_e32 v30, v30
	v_add_f32_e32 v28, 1.0, v28
	v_rcp_f32_e32 v71, v28
	v_lshlrev_b32_e32 v28, 16, v29
	v_add_f32_e32 v30, 1.0, v30
	v_rcp_f32_e32 v75, v30
	v_and_b32_e32 v29, 0xffff0000, v29
	v_pk_mul_f32 v[68:69], v[70:71], v[68:69]
	v_mul_f32_e32 v70, 0xbfb8aa3b, v28
	v_mul_f32_e32 v71, 0xbfb8aa3b, v29
	v_lshlrev_b32_e32 v30, 16, v31
	v_and_b32_e32 v31, 0xffff0000, v31
	v_exp_f32_e32 v70, v70
	v_exp_f32_e32 v71, v71
	v_pk_mul_f32 v[72:73], v[74:75], v[72:73]
	v_mul_f32_e32 v74, 0xbfb8aa3b, v30
	v_mul_f32_e32 v75, 0xbfb8aa3b, v31
	v_exp_f32_e32 v74, v74
	v_exp_f32_e32 v75, v75
	v_add_f32_e32 v70, 1.0, v70
	v_add_f32_e32 v71, 1.0, v71
	v_rcp_f32_e32 v70, v70
	v_rcp_f32_e32 v71, v71
	v_add_f32_e32 v74, 1.0, v74
	v_add_f32_e32 v75, 1.0, v75
	v_rcp_f32_e32 v74, v74
	v_rcp_f32_e32 v75, v75
	v_pk_mul_f32 v[26:27], v[38:39], v[38:39]
	s_waitcnt lgkmcnt(3)
	v_lshlrev_b32_e32 v38, 16, v32
	v_and_b32_e32 v39, 0xffff0000, v32
	v_lshlrev_b32_e32 v32, 16, v33
	v_and_b32_e32 v33, 0xffff0000, v33
	v_pk_mul_f32 v[28:29], v[70:71], v[28:29]
	v_pk_mul_f32 v[30:31], v[74:75], v[30:31]
	v_pk_mul_f32 v[70:71], v[28:29], v[32:33]
	v_lshlrev_b32_e32 v32, 16, v34
	v_and_b32_e32 v33, 0xffff0000, v34
	v_lshlrev_b32_e32 v34, 16, v35
	v_and_b32_e32 v35, 0xffff0000, v35
	v_pk_mul_f32 v[68:69], v[68:69], v[38:39]
	v_pk_mul_f32 v[72:73], v[72:73], v[32:33]
	v_pk_mul_f32 v[34:35], v[30:31], v[34:35]
	v_pk_mul_f32 v[38:39], v[68:69], v[68:69]
	v_pk_mul_f32 v[28:29], v[70:71], v[70:71]
	v_cvt_pk_bf16_f32 v68, v68, v69
	v_cvt_pk_bf16_f32 v69, v70, v71
	v_cvt_pk_bf16_f32 v70, v72, v73
	v_cvt_pk_bf16_f32 v71, v34, v35
	global_store_dwordx4 v[60:61], v[68:71], off offset:2112
	v_pk_mul_f32 v[32:33], v[72:73], v[72:73]
	v_lshlrev_b32_e32 v72, 16, v18
	v_lshlrev_b32_e32 v68, 16, v16
	v_and_b32_e32 v69, 0xffff0000, v16
	v_mul_f32_e32 v16, 0xbfb8aa3b, v68
	v_exp_f32_e32 v16, v16
	v_and_b32_e32 v73, 0xffff0000, v18
	v_mul_f32_e32 v18, 0xbfb8aa3b, v72
	v_exp_f32_e32 v18, v18
	v_add_f32_e32 v16, 1.0, v16
	v_rcp_f32_e32 v70, v16
	v_mul_f32_e32 v16, 0xbfb8aa3b, v69
	v_add_f32_e32 v18, 1.0, v18
	v_exp_f32_e32 v16, v16
	v_rcp_f32_e32 v74, v18
	v_mul_f32_e32 v18, 0xbfb8aa3b, v73
	v_exp_f32_e32 v18, v18
	v_add_f32_e32 v16, 1.0, v16
	v_rcp_f32_e32 v71, v16
	v_lshlrev_b32_e32 v16, 16, v17
	v_add_f32_e32 v18, 1.0, v18
	v_rcp_f32_e32 v75, v18
	v_and_b32_e32 v17, 0xffff0000, v17
	v_pk_mul_f32 v[68:69], v[70:71], v[68:69]
	v_mul_f32_e32 v70, 0xbfb8aa3b, v16
	v_mul_f32_e32 v71, 0xbfb8aa3b, v17
	v_lshlrev_b32_e32 v18, 16, v19
	v_and_b32_e32 v19, 0xffff0000, v19
	v_exp_f32_e32 v70, v70
	v_exp_f32_e32 v71, v71
	v_pk_mul_f32 v[72:73], v[74:75], v[72:73]
	v_mul_f32_e32 v74, 0xbfb8aa3b, v18
	v_mul_f32_e32 v75, 0xbfb8aa3b, v19
	v_exp_f32_e32 v74, v74
	v_exp_f32_e32 v75, v75
	v_add_f32_e32 v70, 1.0, v70
	v_add_f32_e32 v71, 1.0, v71
	v_rcp_f32_e32 v70, v70
	v_rcp_f32_e32 v71, v71
	v_add_f32_e32 v74, 1.0, v74
	v_add_f32_e32 v75, 1.0, v75
	v_rcp_f32_e32 v74, v74
	v_rcp_f32_e32 v75, v75
	v_pk_mul_f32 v[30:31], v[34:35], v[34:35]
	s_waitcnt lgkmcnt(2)
	v_lshlrev_b32_e32 v34, 16, v20
	v_and_b32_e32 v35, 0xffff0000, v20
	v_lshlrev_b32_e32 v20, 16, v21
	v_and_b32_e32 v21, 0xffff0000, v21
	v_pk_mul_f32 v[16:17], v[70:71], v[16:17]
	v_pk_mul_f32 v[18:19], v[74:75], v[18:19]
	v_pk_mul_f32 v[70:71], v[16:17], v[20:21]
	v_lshlrev_b32_e32 v20, 16, v22
	v_and_b32_e32 v21, 0xffff0000, v22
	v_lshlrev_b32_e32 v22, 16, v23
	v_and_b32_e32 v23, 0xffff0000, v23
	v_pk_mul_f32 v[68:69], v[68:69], v[34:35]
	v_pk_mul_f32 v[72:73], v[72:73], v[20:21]
	v_pk_mul_f32 v[22:23], v[18:19], v[22:23]
	v_pk_mul_f32 v[34:35], v[68:69], v[68:69]
	v_pk_mul_f32 v[16:17], v[70:71], v[70:71]
	v_cvt_pk_bf16_f32 v68, v68, v69
	v_cvt_pk_bf16_f32 v69, v70, v71
	v_cvt_pk_bf16_f32 v70, v72, v73
	v_cvt_pk_bf16_f32 v71, v22, v23
	global_store_dwordx4 v[60:61], v[68:71], off offset:2128
	v_pk_mul_f32 v[20:21], v[72:73], v[72:73]
	v_lshlrev_b32_e32 v72, 16, v10
	v_lshlrev_b32_e32 v68, 16, v8
	v_and_b32_e32 v69, 0xffff0000, v8
	v_mul_f32_e32 v8, 0xbfb8aa3b, v68
	v_exp_f32_e32 v8, v8
	v_and_b32_e32 v73, 0xffff0000, v10
	v_mul_f32_e32 v10, 0xbfb8aa3b, v72
	v_exp_f32_e32 v10, v10
	v_add_f32_e32 v62, v62, v63
	v_add_f32_e32 v52, v52, v62
	v_add_f32_e32 v8, 1.0, v8
	v_add_f32_e32 v52, v53, v52
	v_rcp_f32_e32 v70, v8
	v_mul_f32_e32 v8, 0xbfb8aa3b, v69
	v_add_f32_e32 v10, 1.0, v10
	v_add_f32_e32 v52, v64, v52
	v_exp_f32_e32 v8, v8
	v_rcp_f32_e32 v74, v10
	v_mul_f32_e32 v10, 0xbfb8aa3b, v73
	v_add_f32_e32 v52, v65, v52
	v_exp_f32_e32 v10, v10
	v_add_f32_e32 v52, v54, v52
	v_add_f32_e32 v52, v55, v52
	v_add_f32_e32 v52, v66, v52
	v_add_f32_e32 v8, 1.0, v8
	v_add_f32_e32 v52, v67, v52
	v_rcp_f32_e32 v71, v8
	v_add_f32_e32 v10, 1.0, v10
	v_add_f32_e32 v48, v48, v52
	v_rcp_f32_e32 v75, v10
	v_add_f32_e32 v48, v49, v48
	v_add_f32_e32 v48, v56, v48
	v_lshlrev_b32_e32 v8, 16, v9
	v_and_b32_e32 v9, 0xffff0000, v9
	v_add_f32_e32 v48, v57, v48
	v_pk_mul_f32 v[68:69], v[70:71], v[68:69]
	v_mul_f32_e32 v70, 0xbfb8aa3b, v8
	v_mul_f32_e32 v71, 0xbfb8aa3b, v9
	v_lshlrev_b32_e32 v10, 16, v11
	v_and_b32_e32 v11, 0xffff0000, v11
	v_add_f32_e32 v48, v50, v48
	v_exp_f32_e32 v70, v70
	v_exp_f32_e32 v71, v71
	v_pk_mul_f32 v[72:73], v[74:75], v[72:73]
	v_mul_f32_e32 v74, 0xbfb8aa3b, v10
	v_mul_f32_e32 v75, 0xbfb8aa3b, v11
	v_add_f32_e32 v48, v51, v48
	v_exp_f32_e32 v74, v74
	v_exp_f32_e32 v75, v75
	v_add_f32_e32 v48, v58, v48
	v_add_f32_e32 v48, v59, v48
	v_add_f32_e32 v40, v40, v48
	v_add_f32_e32 v70, 1.0, v70
	v_add_f32_e32 v71, 1.0, v71
	v_add_f32_e32 v40, v41, v40
	v_rcp_f32_e32 v70, v70
	v_rcp_f32_e32 v71, v71
	v_add_f32_e32 v74, 1.0, v74
	v_add_f32_e32 v75, 1.0, v75
	v_add_f32_e32 v40, v44, v40
	v_rcp_f32_e32 v74, v74
	v_rcp_f32_e32 v75, v75
	v_add_f32_e32 v40, v45, v40
	v_add_f32_e32 v40, v42, v40
	v_add_f32_e32 v40, v43, v40
	v_pk_mul_f32 v[18:19], v[22:23], v[22:23]
	s_waitcnt lgkmcnt(1)
	v_lshlrev_b32_e32 v22, 16, v12
	v_and_b32_e32 v23, 0xffff0000, v12
	v_lshlrev_b32_e32 v12, 16, v13
	v_and_b32_e32 v13, 0xffff0000, v13
	v_pk_mul_f32 v[8:9], v[70:71], v[8:9]
	v_add_f32_e32 v40, v46, v40
	v_pk_mul_f32 v[70:71], v[8:9], v[12:13]
	v_lshlrev_b32_e32 v12, 16, v14
	v_and_b32_e32 v13, 0xffff0000, v14
	v_lshlrev_b32_e32 v14, 16, v15
	v_and_b32_e32 v15, 0xffff0000, v15
	v_pk_mul_f32 v[10:11], v[74:75], v[10:11]
	v_add_f32_e32 v40, v47, v40
	v_pk_mul_f32 v[68:69], v[68:69], v[22:23]
	v_pk_mul_f32 v[72:73], v[72:73], v[12:13]
	v_pk_mul_f32 v[14:15], v[10:11], v[14:15]
	v_add_f32_e32 v24, v24, v40
	v_pk_mul_f32 v[22:23], v[68:69], v[68:69]
	v_pk_mul_f32 v[8:9], v[70:71], v[70:71]
	v_cvt_pk_bf16_f32 v68, v68, v69
	v_cvt_pk_bf16_f32 v69, v70, v71
	v_cvt_pk_bf16_f32 v70, v72, v73
	v_cvt_pk_bf16_f32 v71, v14, v15
	v_add_f32_e32 v24, v25, v24
	global_store_dwordx4 v[60:61], v[68:71], off offset:2144
	v_add_f32_e32 v24, v36, v24
	v_add_f32_e32 v24, v37, v24
	v_lshlrev_b32_e32 v68, 16, v0
	v_and_b32_e32 v69, 0xffff0000, v0
	v_mul_f32_e32 v0, 0xbfb8aa3b, v68
	v_exp_f32_e32 v0, v0
	v_add_f32_e32 v24, v26, v24
	v_add_f32_e32 v24, v27, v24
	v_pk_mul_f32 v[12:13], v[72:73], v[72:73]
	v_lshlrev_b32_e32 v72, 16, v2
	v_add_f32_e32 v24, v38, v24
	v_and_b32_e32 v73, 0xffff0000, v2
	v_mul_f32_e32 v2, 0xbfb8aa3b, v72
	v_add_f32_e32 v24, v39, v24
	v_add_f32_e32 v0, 1.0, v0
	v_exp_f32_e32 v2, v2
	v_add_f32_e32 v24, v28, v24
	v_rcp_f32_e32 v70, v0
	v_mul_f32_e32 v0, 0xbfb8aa3b, v69
	v_add_f32_e32 v24, v29, v24
	v_exp_f32_e32 v0, v0
	v_add_f32_e32 v24, v32, v24
	v_add_f32_e32 v24, v33, v24
	v_add_f32_e32 v2, 1.0, v2
	v_add_f32_e32 v24, v30, v24
	v_rcp_f32_e32 v74, v2
	v_mul_f32_e32 v2, 0xbfb8aa3b, v73
	v_add_f32_e32 v24, v31, v24
	v_add_f32_e32 v0, 1.0, v0
	v_exp_f32_e32 v2, v2
	v_add_f32_e32 v24, v34, v24
	v_rcp_f32_e32 v71, v0
	v_add_f32_e32 v24, v35, v24
	v_add_f32_e32 v16, v16, v24
	v_add_f32_e32 v16, v17, v16
	v_lshlrev_b32_e32 v0, 16, v1
	v_and_b32_e32 v1, 0xffff0000, v1
	v_add_f32_e32 v2, 1.0, v2
	v_add_f32_e32 v16, v20, v16
	v_pk_mul_f32 v[68:69], v[70:71], v[68:69]
	v_mul_f32_e32 v70, 0xbfb8aa3b, v0
	v_mul_f32_e32 v71, 0xbfb8aa3b, v1
	v_rcp_f32_e32 v75, v2
	v_add_f32_e32 v16, v21, v16
	v_exp_f32_e32 v70, v70
	v_exp_f32_e32 v71, v71
	v_add_f32_e32 v16, v18, v16
	v_add_f32_e32 v16, v19, v16
	v_lshlrev_b32_e32 v2, 16, v3
	v_and_b32_e32 v3, 0xffff0000, v3
	v_add_f32_e32 v16, v22, v16
	v_pk_mul_f32 v[72:73], v[74:75], v[72:73]
	v_mul_f32_e32 v74, 0xbfb8aa3b, v2
	v_mul_f32_e32 v75, 0xbfb8aa3b, v3
	v_add_f32_e32 v16, v23, v16
	v_add_f32_e32 v70, 1.0, v70
	v_add_f32_e32 v71, 1.0, v71
	v_exp_f32_e32 v74, v74
	v_exp_f32_e32 v75, v75
	v_add_f32_e32 v8, v8, v16
	v_rcp_f32_e32 v70, v70
	v_rcp_f32_e32 v71, v71
	v_add_f32_e32 v8, v9, v8
	v_add_f32_e32 v8, v12, v8
	v_pk_mul_f32 v[10:11], v[14:15], v[14:15]
	s_waitcnt lgkmcnt(0)
	v_lshlrev_b32_e32 v14, 16, v4
	v_and_b32_e32 v15, 0xffff0000, v4
	v_add_f32_e32 v8, v13, v8
	v_pk_mul_f32 v[14:15], v[68:69], v[14:15]
	v_add_f32_e32 v74, 1.0, v74
	v_add_f32_e32 v75, 1.0, v75
	v_add_f32_e32 v8, v10, v8
	v_pk_mul_f32 v[68:69], v[14:15], v[14:15]
	v_lshlrev_b32_e32 v4, 16, v5
	v_and_b32_e32 v5, 0xffff0000, v5
	v_pk_mul_f32 v[0:1], v[70:71], v[0:1]
	v_rcp_f32_e32 v74, v74
	v_rcp_f32_e32 v75, v75
	v_add_f32_e32 v8, v11, v8
	v_pk_mul_f32 v[4:5], v[0:1], v[4:5]
	v_add_f32_e32 v8, v68, v8
	v_pk_mul_f32 v[0:1], v[4:5], v[4:5]
	v_lshlrev_b32_e32 v70, 16, v6
	v_and_b32_e32 v71, 0xffff0000, v6
	v_add_f32_e32 v8, v69, v8
	v_pk_mul_f32 v[70:71], v[72:73], v[70:71]
	v_add_f32_e32 v0, v0, v8
	v_pk_mul_f32 v[72:73], v[70:71], v[70:71]
	v_lshlrev_b32_e32 v6, 16, v7
	v_and_b32_e32 v7, 0xffff0000, v7
	v_pk_mul_f32 v[2:3], v[74:75], v[2:3]
	v_add_f32_e32 v0, v1, v0
	v_pk_mul_f32 v[6:7], v[2:3], v[6:7]
	v_add_f32_e32 v0, v72, v0
	v_pk_mul_f32 v[2:3], v[6:7], v[6:7]
	v_add_f32_e32 v0, v73, v0
	v_add_f32_e32 v0, v2, v0
	v_add_f32_e32 v8, v3, v0
	v_cvt_pk_bf16_f32 v0, v14, v15
	v_cvt_pk_bf16_f32 v1, v4, v5
	v_cvt_pk_bf16_f32 v2, v70, v71
	v_cvt_pk_bf16_f32 v3, v6, v7
	global_store_dwordx4 v[60:61], v[0:3], off offset:2160
	ds_write_b32 v156, v8
	s_waitcnt lgkmcnt(0)
	s_barrier
	s_and_saveexec_b64 vcc, s[66:67]
	s_cbranch_execz .LBB0_640
	ds_read2st64_b32 v[0:1], v140 offset1:1
	v_readlane_b32 s12, v253, 57
	v_readlane_b32 s13, v253, 58
	s_waitcnt lgkmcnt(0)
	v_add_f32_e32 v0, 0, v0
	v_add_f32_e32 v2, v0, v1
	ds_read2st64_b32 v[0:1], v140 offset0:2 offset1:3
	s_waitcnt lgkmcnt(0)
	v_add_f32_e32 v0, v2, v0
	v_add_f32_e32 v2, v0, v1
	ds_read2st64_b32 v[0:1], v140 offset0:4 offset1:5
	s_waitcnt lgkmcnt(0)
	v_add_f32_e32 v0, v2, v0
	v_add_f32_e32 v2, v0, v1
	ds_read2st64_b32 v[0:1], v140 offset0:6 offset1:7
	s_waitcnt lgkmcnt(0)
	v_add_f32_e32 v0, v2, v0
	v_add_f32_e32 v0, v0, v1
	v_fmamk_f32 v0, v0, 0x3b000000, v222
	v_rsq_f32_e32 v2, v0
	v_add_u32_e32 v0, s20, v133
	v_ashrrev_i32_e32 v1, 31, v0
	v_lshl_add_u64 v[0:1], v[0:1], 2, s[12:13]
	global_store_dword v[0:1], v2, off
	s_branch .LBB0_640
